# speedup vs baseline: 1.0153x; 1.0063x over previous
.LBB0_8:
	s_load_dwordx4 s[8:11], s[0:1], 0x0
	s_load_dwordx2 s[12:13], s[0:1], 0x10
	v_lshrrev_b32_e32 v6, 6, v0
	v_lshl_or_b32 v1, s2, 2, v6
	s_movk_i32 s0, 0xc2
	v_and_b32_e32 v28, 63, v0
	v_mul_lo_u32 v2, v1, s0
	v_mov_b32_e32 v3, 0
	s_waitcnt lgkmcnt(0)
	v_lshl_add_u64 v[4:5], v[2:3], 2, s[10:11]
	v_lshlrev_b32_e32 v2, 2, v28
	v_lshl_add_u64 v[4:5], v[4:5], 0, v[2:3]
	global_load_dword v7, v[4:5], off nt
	global_load_dword v8, v[4:5], off offset:256 nt
	global_load_dword v9, v[4:5], off offset:512 nt
	v_lshlrev_b32_e32 v30, 10, v6
	v_or_b32_e32 v2, v30, v2
	v_cmp_gt_u32_e32 vcc, 2, v28
	s_and_saveexec_b64 s[0:1], vcc
	s_cbranch_execz .Lsim_notail
	global_load_dword v56, v[4:5], off offset:768 nt
.Lsim_notail:
	s_or_b64 exec, exec, s[0:1]
	v_lshl_or_b32 v58, v1, 8, v28
	v_mov_b32_e32 v59, 0
	v_lshl_add_u64 v[58:59], v[58:59], 2, s[8:9]
	global_load_dword v54, v[58:59], off nt
	global_load_dword v53, v[58:59], off offset:256 nt
	global_load_dword v52, v[58:59], off offset:512 nt
	global_load_dword v55, v[58:59], off offset:768 nt
	s_waitcnt vmcnt(5)
	ds_write2st64_b32 v2, v7, v8 offset1:1
	ds_write_b32 v2, v9 offset:512
	s_waitcnt vmcnt(4)
	s_and_saveexec_b64 s[0:1], vcc
	s_cbranch_execz .LBB0_10
	ds_write_b32 v2, v56 offset:768
